# PLE epilogue arithmetic packed as well (v_pk_mul/add/fma_f32 on element pairs, -log2e from an SGPR pair), on top of the packed RG gate epilogue
# speedup vs baseline: 1.0027x; 1.0027x over previous
.LBB0_741:
	v_mov_b32_e32 v2, v0
	s_nop 15
	s_nop 15
	s_movk_i32 s6, 0xffc0
	v_bfe_u32 v26, v2, 6, 2
	v_and_b32_e32 v3, 15, v2
	v_bfe_u32 v27, v2, 4, 2
	v_ashrrev_i32_e32 v2, 2, v2
	v_and_or_b32 v48, v2, s6, v3
	v_lshlrev_b32_e32 v2, 3, v27
	v_lshl_or_b32 v34, v26, 5, v2
	s_cmp_lt_i32 s1, 7
	s_mov_b64 s[6:7], -1
	s_cbranch_scc1 .LBB0_765
	s_cmp_lt_i32 s1, 8
	s_cbranch_scc1 .LBB0_762
	s_cmp_eq_u32 s1, 8
	s_cbranch_scc0 .LBB0_761
	v_lshl_add_u32 v50, s36, 8, v48
	v_ashrrev_i32_e32 v51, 31, v50
	s_lshl_b32 s6, s44, 8
	v_lshlrev_b64 v[52:53], 10, v[50:51]
	s_ashr_i32 s7, s6, 31
	v_lshl_add_u64 v[52:53], v[52:53], 0, s[6:7]
	v_or_b32_e32 v52, v52, v34
	v_lshlrev_b64 v[52:53], 1, v[52:53]
	v_lshl_add_u64 v[58:59], s[50:51], 0, v[52:53]
	v_lshl_add_u64 v[60:61], s[54:55], 0, v[52:53]
	v_lshl_add_u64 v[62:63], s[50:51], 0, v[52:53]
	v_lshlrev_b32_e32 v66, 2, v26
	s_lshl_b32 s6, s44, 2
	s_ashr_i32 s7, s6, 31
	s_lshl_b64 s[6:7], s[6:7], 2
	s_add_u32 s6, s56, s6
	s_addc_u32 s7, s57, s7
	v_lshl_add_u64 v[64:65], s[6:7], 0, v[66:67]
	v_lshlrev_b64 v[52:53], 6, v[50:51]
	v_lshl_add_u64 v[64:65], v[64:65], 0, v[52:53]
	s_mov_b32 s42, 0xbfb8aa3b
	s_mov_b32 s43, 0xbfb8aa3b
	global_load_dwordx4 v[2:5], v[58:59], off
	global_load_dwordx4 v[6:9], v[58:59], off offset:256
	global_load_dwordx4 v[10:13], v[60:61], off
	global_load_dwordx4 v[14:17], v[60:61], off offset:256
	v_add_co_u32_e32 v58, vcc, 0x8000, v58
	s_nop 1
	v_addc_co_u32_e32 v59, vcc, 0, v59, vcc
	v_add_co_u32_e32 v60, vcc, 0x8000, v60
	s_nop 1
	v_addc_co_u32_e32 v61, vcc, 0, v61, vcc
	global_load_dwordx4 v[18:21], v[58:59], off
	global_load_dwordx4 v[22:25], v[58:59], off offset:256
	global_load_dwordx4 v[26:29], v[60:61], off
	global_load_dwordx4 v[30:33], v[60:61], off offset:256
	v_add_co_u32_e32 v58, vcc, 0x8000, v58
	s_nop 1
	v_addc_co_u32_e32 v59, vcc, 0, v59, vcc
	v_add_co_u32_e32 v60, vcc, 0x8000, v60
	s_nop 1
	v_addc_co_u32_e32 v61, vcc, 0, v61, vcc
	global_load_dwordx4 v[34:37], v[58:59], off
	global_load_dwordx4 v[38:41], v[58:59], off offset:256
	global_load_dwordx4 v[42:45], v[60:61], off
	global_load_dwordx4 v[46:49], v[60:61], off offset:256
	v_add_co_u32_e32 v58, vcc, 0x8000, v58
	s_nop 1
	v_addc_co_u32_e32 v59, vcc, 0, v59, vcc
	v_add_co_u32_e32 v60, vcc, 0x8000, v60
	s_nop 1
	v_addc_co_u32_e32 v61, vcc, 0, v61, vcc
	s_waitcnt vmcnt(8)
	v_pk_mul_f32 v[72:73], v[72:73], s[42:43]
	v_pk_mul_f32 v[74:75], v[74:75], s[42:43]
	v_exp_f32_e32 v72, v72
	v_exp_f32_e32 v73, v73
	v_exp_f32_e32 v74, v74
	v_exp_f32_e32 v75, v75
	v_pk_add_f32 v[72:73], v[72:73], 1.0 op_sel_hi:[1,0]
	v_pk_add_f32 v[74:75], v[74:75], 1.0 op_sel_hi:[1,0]
	v_rcp_f32_e32 v72, v72
	v_rcp_f32_e32 v73, v73
	v_rcp_f32_e32 v74, v74
	v_rcp_f32_e32 v75, v75
	v_lshlrev_b32_e32 v50, 16, v2
	v_and_b32_e32 v51, 0xffff0000, v2
	v_lshlrev_b32_e32 v52, 16, v3
	v_and_b32_e32 v53, 0xffff0000, v3
	v_lshlrev_b32_e32 v54, 16, v10
	v_and_b32_e32 v55, 0xffff0000, v10
	v_lshlrev_b32_e32 v56, 16, v11
	v_and_b32_e32 v57, 0xffff0000, v11
	v_pk_fma_f32 v[50:51], v[72:73], v[54:55], v[50:51]
	v_pk_fma_f32 v[52:53], v[74:75], v[56:57], v[52:53]
	v_cvt_pk_bf16_f32 v2, v50, v51
	v_cvt_pk_bf16_f32 v3, v52, v53
	v_pk_mul_f32 v[10:11], v[50:51], v[50:51]
	v_pk_fma_f32 v[10:11], v[52:53], v[52:53], v[10:11]
	v_pk_mul_f32 v[192:193], v[192:193], s[42:43]
	v_pk_mul_f32 v[194:195], v[194:195], s[42:43]
	v_exp_f32_e32 v192, v192
	v_exp_f32_e32 v193, v193
	v_exp_f32_e32 v194, v194
	v_exp_f32_e32 v195, v195
	v_pk_add_f32 v[192:193], v[192:193], 1.0 op_sel_hi:[1,0]
	v_pk_add_f32 v[194:195], v[194:195], 1.0 op_sel_hi:[1,0]
	v_rcp_f32_e32 v192, v192
	v_rcp_f32_e32 v193, v193
	v_rcp_f32_e32 v194, v194
	v_rcp_f32_e32 v195, v195
	v_lshlrev_b32_e32 v50, 16, v4
	v_and_b32_e32 v51, 0xffff0000, v4
	v_lshlrev_b32_e32 v52, 16, v5
	v_and_b32_e32 v53, 0xffff0000, v5
	v_lshlrev_b32_e32 v54, 16, v12
	v_and_b32_e32 v55, 0xffff0000, v12
	v_lshlrev_b32_e32 v56, 16, v13
	v_and_b32_e32 v57, 0xffff0000, v13
	v_pk_fma_f32 v[50:51], v[192:193], v[54:55], v[50:51]
	v_pk_fma_f32 v[52:53], v[194:195], v[56:57], v[52:53]
	v_cvt_pk_bf16_f32 v4, v50, v51
	v_cvt_pk_bf16_f32 v5, v52, v53
	v_pk_fma_f32 v[10:11], v[50:51], v[50:51], v[10:11]
	v_pk_fma_f32 v[10:11], v[52:53], v[52:53], v[10:11]
	v_pk_mul_f32 v[164:165], v[164:165], s[42:43]
	v_pk_mul_f32 v[166:167], v[166:167], s[42:43]
	v_exp_f32_e32 v164, v164
	v_exp_f32_e32 v165, v165
	v_exp_f32_e32 v166, v166
	v_exp_f32_e32 v167, v167
	v_pk_add_f32 v[164:165], v[164:165], 1.0 op_sel_hi:[1,0]
	v_pk_add_f32 v[166:167], v[166:167], 1.0 op_sel_hi:[1,0]
	v_rcp_f32_e32 v164, v164
	v_rcp_f32_e32 v165, v165
	v_rcp_f32_e32 v166, v166
	v_rcp_f32_e32 v167, v167
	v_lshlrev_b32_e32 v50, 16, v6
	v_and_b32_e32 v51, 0xffff0000, v6
	v_lshlrev_b32_e32 v52, 16, v7
	v_and_b32_e32 v53, 0xffff0000, v7
	v_lshlrev_b32_e32 v54, 16, v14
	v_and_b32_e32 v55, 0xffff0000, v14
	v_lshlrev_b32_e32 v56, 16, v15
	v_and_b32_e32 v57, 0xffff0000, v15
	v_pk_fma_f32 v[50:51], v[164:165], v[54:55], v[50:51]
	v_pk_fma_f32 v[52:53], v[166:167], v[56:57], v[52:53]
	v_cvt_pk_bf16_f32 v6, v50, v51
	v_cvt_pk_bf16_f32 v7, v52, v53
	v_pk_fma_f32 v[10:11], v[50:51], v[50:51], v[10:11]
	v_pk_fma_f32 v[10:11], v[52:53], v[52:53], v[10:11]
	v_pk_mul_f32 v[160:161], v[160:161], s[42:43]
	v_pk_mul_f32 v[162:163], v[162:163], s[42:43]
	v_exp_f32_e32 v160, v160
	v_exp_f32_e32 v161, v161
	v_exp_f32_e32 v162, v162
	v_exp_f32_e32 v163, v163
	v_pk_add_f32 v[160:161], v[160:161], 1.0 op_sel_hi:[1,0]
	v_pk_add_f32 v[162:163], v[162:163], 1.0 op_sel_hi:[1,0]
	v_rcp_f32_e32 v160, v160
	v_rcp_f32_e32 v161, v161
	v_rcp_f32_e32 v162, v162
	v_rcp_f32_e32 v163, v163
	v_lshlrev_b32_e32 v50, 16, v8
	v_and_b32_e32 v51, 0xffff0000, v8
	v_lshlrev_b32_e32 v52, 16, v9
	v_and_b32_e32 v53, 0xffff0000, v9
	v_lshlrev_b32_e32 v54, 16, v16
	v_and_b32_e32 v55, 0xffff0000, v16
	v_lshlrev_b32_e32 v56, 16, v17
	v_and_b32_e32 v57, 0xffff0000, v17
	v_pk_fma_f32 v[50:51], v[160:161], v[54:55], v[50:51]
	v_pk_fma_f32 v[52:53], v[162:163], v[56:57], v[52:53]
	v_cvt_pk_bf16_f32 v8, v50, v51
	v_cvt_pk_bf16_f32 v9, v52, v53
	v_pk_fma_f32 v[10:11], v[50:51], v[50:51], v[10:11]
	v_pk_fma_f32 v[10:11], v[52:53], v[52:53], v[10:11]
	v_add_f32_e32 v10, v10, v11
	global_load_dwordx4 v[72:75], v[58:59], off
	global_load_dwordx4 v[192:195], v[58:59], off offset:256
	global_load_dwordx4 v[164:167], v[60:61], off
	global_load_dwordx4 v[160:163], v[60:61], off offset:256
	v_add_co_u32_e32 v58, vcc, 0x28000, v58
	s_nop 1
	v_addc_co_u32_e32 v59, vcc, 0, v59, vcc
	v_add_co_u32_e32 v60, vcc, 0x28000, v60
	s_nop 1
	v_addc_co_u32_e32 v61, vcc, 0, v61, vcc
	global_store_dwordx4 v[62:63], v[2:5], off
	global_store_dwordx4 v[62:63], v[6:9], off offset:256
	v_add_co_u32_e32 v62, vcc, 0x8000, v62
	s_nop 1
	v_addc_co_u32_e32 v63, vcc, 0, v63, vcc
	s_waitcnt vmcnt(10)
	v_pk_mul_f32 v[188:189], v[188:189], s[42:43]
	v_pk_mul_f32 v[190:191], v[190:191], s[42:43]
	v_exp_f32_e32 v188, v188
	v_exp_f32_e32 v189, v189
	v_exp_f32_e32 v190, v190
	v_exp_f32_e32 v191, v191
	v_pk_add_f32 v[188:189], v[188:189], 1.0 op_sel_hi:[1,0]
	v_pk_add_f32 v[190:191], v[190:191], 1.0 op_sel_hi:[1,0]
	v_rcp_f32_e32 v188, v188
	v_rcp_f32_e32 v189, v189
	v_rcp_f32_e32 v190, v190
	v_rcp_f32_e32 v191, v191
	v_lshlrev_b32_e32 v50, 16, v18
	v_and_b32_e32 v51, 0xffff0000, v18
	v_lshlrev_b32_e32 v52, 16, v19
	v_and_b32_e32 v53, 0xffff0000, v19
	v_lshlrev_b32_e32 v54, 16, v26
	v_and_b32_e32 v55, 0xffff0000, v26
	v_lshlrev_b32_e32 v56, 16, v27
	v_and_b32_e32 v57, 0xffff0000, v27
	v_pk_fma_f32 v[50:51], v[188:189], v[54:55], v[50:51]
	v_pk_fma_f32 v[52:53], v[190:191], v[56:57], v[52:53]
	v_cvt_pk_bf16_f32 v18, v50, v51
	v_cvt_pk_bf16_f32 v19, v52, v53
	v_pk_mul_f32 v[26:27], v[50:51], v[50:51]
	v_pk_fma_f32 v[26:27], v[52:53], v[52:53], v[26:27]
	v_pk_mul_f32 v[184:185], v[184:185], s[42:43]
	v_pk_mul_f32 v[186:187], v[186:187], s[42:43]
	v_exp_f32_e32 v184, v184
	v_exp_f32_e32 v185, v185
	v_exp_f32_e32 v186, v186
	v_exp_f32_e32 v187, v187
	v_pk_add_f32 v[184:185], v[184:185], 1.0 op_sel_hi:[1,0]
	v_pk_add_f32 v[186:187], v[186:187], 1.0 op_sel_hi:[1,0]
	v_rcp_f32_e32 v184, v184
	v_rcp_f32_e32 v185, v185
	v_rcp_f32_e32 v186, v186
	v_rcp_f32_e32 v187, v187
	v_lshlrev_b32_e32 v50, 16, v20
	v_and_b32_e32 v51, 0xffff0000, v20
	v_lshlrev_b32_e32 v52, 16, v21
	v_and_b32_e32 v53, 0xffff0000, v21
	v_lshlrev_b32_e32 v54, 16, v28
	v_and_b32_e32 v55, 0xffff0000, v28
	v_lshlrev_b32_e32 v56, 16, v29
	v_and_b32_e32 v57, 0xffff0000, v29
	v_pk_fma_f32 v[50:51], v[184:185], v[54:55], v[50:51]
	v_pk_fma_f32 v[52:53], v[186:187], v[56:57], v[52:53]
	v_cvt_pk_bf16_f32 v20, v50, v51
	v_cvt_pk_bf16_f32 v21, v52, v53
	v_pk_fma_f32 v[26:27], v[50:51], v[50:51], v[26:27]
	v_pk_fma_f32 v[26:27], v[52:53], v[52:53], v[26:27]
	v_pk_mul_f32 v[156:157], v[156:157], s[42:43]
	v_pk_mul_f32 v[158:159], v[158:159], s[42:43]
	v_exp_f32_e32 v156, v156
	v_exp_f32_e32 v157, v157
	v_exp_f32_e32 v158, v158
	v_exp_f32_e32 v159, v159
	v_pk_add_f32 v[156:157], v[156:157], 1.0 op_sel_hi:[1,0]
	v_pk_add_f32 v[158:159], v[158:159], 1.0 op_sel_hi:[1,0]
	v_rcp_f32_e32 v156, v156
	v_rcp_f32_e32 v157, v157
	v_rcp_f32_e32 v158, v158
	v_rcp_f32_e32 v159, v159
	v_lshlrev_b32_e32 v50, 16, v22
	v_and_b32_e32 v51, 0xffff0000, v22
	v_lshlrev_b32_e32 v52, 16, v23
	v_and_b32_e32 v53, 0xffff0000, v23
	v_lshlrev_b32_e32 v54, 16, v30
	v_and_b32_e32 v55, 0xffff0000, v30
	v_lshlrev_b32_e32 v56, 16, v31
	v_and_b32_e32 v57, 0xffff0000, v31
	v_pk_fma_f32 v[50:51], v[156:157], v[54:55], v[50:51]
	v_pk_fma_f32 v[52:53], v[158:159], v[56:57], v[52:53]
	v_cvt_pk_bf16_f32 v22, v50, v51
	v_cvt_pk_bf16_f32 v23, v52, v53
	v_pk_fma_f32 v[26:27], v[50:51], v[50:51], v[26:27]
	v_pk_fma_f32 v[26:27], v[52:53], v[52:53], v[26:27]
	v_pk_mul_f32 v[152:153], v[152:153], s[42:43]
	v_pk_mul_f32 v[154:155], v[154:155], s[42:43]
	v_exp_f32_e32 v152, v152
	v_exp_f32_e32 v153, v153
	v_exp_f32_e32 v154, v154
	v_exp_f32_e32 v155, v155
	v_pk_add_f32 v[152:153], v[152:153], 1.0 op_sel_hi:[1,0]
	v_pk_add_f32 v[154:155], v[154:155], 1.0 op_sel_hi:[1,0]
	v_rcp_f32_e32 v152, v152
	v_rcp_f32_e32 v153, v153
	v_rcp_f32_e32 v154, v154
	v_rcp_f32_e32 v155, v155
	v_lshlrev_b32_e32 v50, 16, v24
	v_and_b32_e32 v51, 0xffff0000, v24
	v_lshlrev_b32_e32 v52, 16, v25
	v_and_b32_e32 v53, 0xffff0000, v25
	v_lshlrev_b32_e32 v54, 16, v32
	v_and_b32_e32 v55, 0xffff0000, v32
	v_lshlrev_b32_e32 v56, 16, v33
	v_and_b32_e32 v57, 0xffff0000, v33
	v_pk_fma_f32 v[50:51], v[152:153], v[54:55], v[50:51]
	v_pk_fma_f32 v[52:53], v[154:155], v[56:57], v[52:53]
	v_cvt_pk_bf16_f32 v24, v50, v51
	v_cvt_pk_bf16_f32 v25, v52, v53
	v_pk_fma_f32 v[26:27], v[50:51], v[50:51], v[26:27]
	v_pk_fma_f32 v[26:27], v[52:53], v[52:53], v[26:27]
	v_add_f32_e32 v26, v26, v27
	global_load_dwordx4 v[188:191], v[58:59], off
	global_load_dwordx4 v[184:187], v[58:59], off offset:256
	global_load_dwordx4 v[156:159], v[60:61], off
	global_load_dwordx4 v[152:155], v[60:61], off offset:256
	v_add_co_u32_e32 v58, vcc, 0x8000, v58
	s_nop 1
	v_addc_co_u32_e32 v59, vcc, 0, v59, vcc
	v_add_co_u32_e32 v60, vcc, 0x8000, v60
	s_nop 1
	v_addc_co_u32_e32 v61, vcc, 0, v61, vcc
	global_store_dwordx4 v[62:63], v[18:21], off
	global_store_dwordx4 v[62:63], v[22:25], off offset:256
	v_add_co_u32_e32 v62, vcc, 0x8000, v62
	s_nop 1
	v_addc_co_u32_e32 v63, vcc, 0, v63, vcc
	s_waitcnt vmcnt(12)
	v_pk_mul_f32 v[180:181], v[180:181], s[42:43]
	v_pk_mul_f32 v[182:183], v[182:183], s[42:43]
	v_exp_f32_e32 v180, v180
	v_exp_f32_e32 v181, v181
	v_exp_f32_e32 v182, v182
	v_exp_f32_e32 v183, v183
	v_pk_add_f32 v[180:181], v[180:181], 1.0 op_sel_hi:[1,0]
	v_pk_add_f32 v[182:183], v[182:183], 1.0 op_sel_hi:[1,0]
	v_rcp_f32_e32 v180, v180
	v_rcp_f32_e32 v181, v181
	v_rcp_f32_e32 v182, v182
	v_rcp_f32_e32 v183, v183
	v_lshlrev_b32_e32 v50, 16, v34
	v_and_b32_e32 v51, 0xffff0000, v34
	v_lshlrev_b32_e32 v52, 16, v35
	v_and_b32_e32 v53, 0xffff0000, v35
	v_lshlrev_b32_e32 v54, 16, v42
	v_and_b32_e32 v55, 0xffff0000, v42
	v_lshlrev_b32_e32 v56, 16, v43
	v_and_b32_e32 v57, 0xffff0000, v43
	v_pk_fma_f32 v[50:51], v[180:181], v[54:55], v[50:51]
	v_pk_fma_f32 v[52:53], v[182:183], v[56:57], v[52:53]
	v_cvt_pk_bf16_f32 v34, v50, v51
	v_cvt_pk_bf16_f32 v35, v52, v53
	v_pk_mul_f32 v[42:43], v[50:51], v[50:51]
	v_pk_fma_f32 v[42:43], v[52:53], v[52:53], v[42:43]
	v_pk_mul_f32 v[176:177], v[176:177], s[42:43]
	v_pk_mul_f32 v[178:179], v[178:179], s[42:43]
	v_exp_f32_e32 v176, v176
	v_exp_f32_e32 v177, v177
	v_exp_f32_e32 v178, v178
	v_exp_f32_e32 v179, v179
	v_pk_add_f32 v[176:177], v[176:177], 1.0 op_sel_hi:[1,0]
	v_pk_add_f32 v[178:179], v[178:179], 1.0 op_sel_hi:[1,0]
	v_rcp_f32_e32 v176, v176
	v_rcp_f32_e32 v177, v177
	v_rcp_f32_e32 v178, v178
	v_rcp_f32_e32 v179, v179
	v_lshlrev_b32_e32 v50, 16, v36
	v_and_b32_e32 v51, 0xffff0000, v36
	v_lshlrev_b32_e32 v52, 16, v37
	v_and_b32_e32 v53, 0xffff0000, v37
	v_lshlrev_b32_e32 v54, 16, v44
	v_and_b32_e32 v55, 0xffff0000, v44
	v_lshlrev_b32_e32 v56, 16, v45
	v_and_b32_e32 v57, 0xffff0000, v45
	v_pk_fma_f32 v[50:51], v[176:177], v[54:55], v[50:51]
	v_pk_fma_f32 v[52:53], v[178:179], v[56:57], v[52:53]
	v_cvt_pk_bf16_f32 v36, v50, v51
	v_cvt_pk_bf16_f32 v37, v52, v53
	v_pk_fma_f32 v[42:43], v[50:51], v[50:51], v[42:43]
	v_pk_fma_f32 v[42:43], v[52:53], v[52:53], v[42:43]
	v_pk_mul_f32 v[148:149], v[148:149], s[42:43]
	v_pk_mul_f32 v[150:151], v[150:151], s[42:43]
	v_exp_f32_e32 v148, v148
	v_exp_f32_e32 v149, v149
	v_exp_f32_e32 v150, v150
	v_exp_f32_e32 v151, v151
	v_pk_add_f32 v[148:149], v[148:149], 1.0 op_sel_hi:[1,0]
	v_pk_add_f32 v[150:151], v[150:151], 1.0 op_sel_hi:[1,0]
	v_rcp_f32_e32 v148, v148
	v_rcp_f32_e32 v149, v149
	v_rcp_f32_e32 v150, v150
	v_rcp_f32_e32 v151, v151
	v_lshlrev_b32_e32 v50, 16, v38
	v_and_b32_e32 v51, 0xffff0000, v38
	v_lshlrev_b32_e32 v52, 16, v39
	v_and_b32_e32 v53, 0xffff0000, v39
	v_lshlrev_b32_e32 v54, 16, v46
	v_and_b32_e32 v55, 0xffff0000, v46
	v_lshlrev_b32_e32 v56, 16, v47
	v_and_b32_e32 v57, 0xffff0000, v47
	v_pk_fma_f32 v[50:51], v[148:149], v[54:55], v[50:51]
	v_pk_fma_f32 v[52:53], v[150:151], v[56:57], v[52:53]
	v_cvt_pk_bf16_f32 v38, v50, v51
	v_cvt_pk_bf16_f32 v39, v52, v53
	v_pk_fma_f32 v[42:43], v[50:51], v[50:51], v[42:43]
	v_pk_fma_f32 v[42:43], v[52:53], v[52:53], v[42:43]
	v_pk_mul_f32 v[144:145], v[144:145], s[42:43]
	v_pk_mul_f32 v[146:147], v[146:147], s[42:43]
	v_exp_f32_e32 v144, v144
	v_exp_f32_e32 v145, v145
	v_exp_f32_e32 v146, v146
	v_exp_f32_e32 v147, v147
	v_pk_add_f32 v[144:145], v[144:145], 1.0 op_sel_hi:[1,0]
	v_pk_add_f32 v[146:147], v[146:147], 1.0 op_sel_hi:[1,0]
	v_rcp_f32_e32 v144, v144
	v_rcp_f32_e32 v145, v145
	v_rcp_f32_e32 v146, v146
	v_rcp_f32_e32 v147, v147
	v_lshlrev_b32_e32 v50, 16, v40
	v_and_b32_e32 v51, 0xffff0000, v40
	v_lshlrev_b32_e32 v52, 16, v41
	v_and_b32_e32 v53, 0xffff0000, v41
	v_lshlrev_b32_e32 v54, 16, v48
	v_and_b32_e32 v55, 0xffff0000, v48
	v_lshlrev_b32_e32 v56, 16, v49
	v_and_b32_e32 v57, 0xffff0000, v49
	v_pk_fma_f32 v[50:51], v[144:145], v[54:55], v[50:51]
	v_pk_fma_f32 v[52:53], v[146:147], v[56:57], v[52:53]
	v_cvt_pk_bf16_f32 v40, v50, v51
	v_cvt_pk_bf16_f32 v41, v52, v53
	v_pk_fma_f32 v[42:43], v[50:51], v[50:51], v[42:43]
	v_pk_fma_f32 v[42:43], v[52:53], v[52:53], v[42:43]
	v_add_f32_e32 v42, v42, v43
	global_load_dwordx4 v[180:183], v[58:59], off
	global_load_dwordx4 v[176:179], v[58:59], off offset:256
	global_load_dwordx4 v[148:151], v[60:61], off
	global_load_dwordx4 v[144:147], v[60:61], off offset:256
	v_add_co_u32_e32 v58, vcc, 0x8000, v58
	s_nop 1
	v_addc_co_u32_e32 v59, vcc, 0, v59, vcc
	v_add_co_u32_e32 v60, vcc, 0x8000, v60
	s_nop 1
	v_addc_co_u32_e32 v61, vcc, 0, v61, vcc
	global_store_dwordx4 v[62:63], v[34:37], off
	global_store_dwordx4 v[62:63], v[38:41], off offset:256
	v_add_co_u32_e32 v62, vcc, 0x8000, v62
	s_nop 1
	v_addc_co_u32_e32 v63, vcc, 0, v63, vcc
	s_waitcnt vmcnt(14)
	v_pk_mul_f32 v[172:173], v[172:173], s[42:43]
	v_pk_mul_f32 v[174:175], v[174:175], s[42:43]
	v_exp_f32_e32 v172, v172
	v_exp_f32_e32 v173, v173
	v_exp_f32_e32 v174, v174
	v_exp_f32_e32 v175, v175
	v_pk_add_f32 v[172:173], v[172:173], 1.0 op_sel_hi:[1,0]
	v_pk_add_f32 v[174:175], v[174:175], 1.0 op_sel_hi:[1,0]
	v_rcp_f32_e32 v172, v172
	v_rcp_f32_e32 v173, v173
	v_rcp_f32_e32 v174, v174
	v_rcp_f32_e32 v175, v175
	v_lshlrev_b32_e32 v50, 16, v72
	v_and_b32_e32 v51, 0xffff0000, v72
	v_lshlrev_b32_e32 v52, 16, v73
	v_and_b32_e32 v53, 0xffff0000, v73
	v_lshlrev_b32_e32 v54, 16, v164
	v_and_b32_e32 v55, 0xffff0000, v164
	v_lshlrev_b32_e32 v56, 16, v165
	v_and_b32_e32 v57, 0xffff0000, v165
	v_pk_fma_f32 v[50:51], v[172:173], v[54:55], v[50:51]
	v_pk_fma_f32 v[52:53], v[174:175], v[56:57], v[52:53]
	v_cvt_pk_bf16_f32 v72, v50, v51
	v_cvt_pk_bf16_f32 v73, v52, v53
	v_pk_mul_f32 v[164:165], v[50:51], v[50:51]
	v_pk_fma_f32 v[164:165], v[52:53], v[52:53], v[164:165]
	v_pk_mul_f32 v[168:169], v[168:169], s[42:43]
	v_pk_mul_f32 v[170:171], v[170:171], s[42:43]
	v_exp_f32_e32 v168, v168
	v_exp_f32_e32 v169, v169
	v_exp_f32_e32 v170, v170
	v_exp_f32_e32 v171, v171
	v_pk_add_f32 v[168:169], v[168:169], 1.0 op_sel_hi:[1,0]
	v_pk_add_f32 v[170:171], v[170:171], 1.0 op_sel_hi:[1,0]
	v_rcp_f32_e32 v168, v168
	v_rcp_f32_e32 v169, v169
	v_rcp_f32_e32 v170, v170
	v_rcp_f32_e32 v171, v171
	v_lshlrev_b32_e32 v50, 16, v74
	v_and_b32_e32 v51, 0xffff0000, v74
	v_lshlrev_b32_e32 v52, 16, v75
	v_and_b32_e32 v53, 0xffff0000, v75
	v_lshlrev_b32_e32 v54, 16, v166
	v_and_b32_e32 v55, 0xffff0000, v166
	v_lshlrev_b32_e32 v56, 16, v167
	v_and_b32_e32 v57, 0xffff0000, v167
	v_pk_fma_f32 v[50:51], v[168:169], v[54:55], v[50:51]
	v_pk_fma_f32 v[52:53], v[170:171], v[56:57], v[52:53]
	v_cvt_pk_bf16_f32 v74, v50, v51
	v_cvt_pk_bf16_f32 v75, v52, v53
	v_pk_fma_f32 v[164:165], v[50:51], v[50:51], v[164:165]
	v_pk_fma_f32 v[164:165], v[52:53], v[52:53], v[164:165]
	v_pk_mul_f32 v[140:141], v[140:141], s[42:43]
	v_pk_mul_f32 v[142:143], v[142:143], s[42:43]
	v_exp_f32_e32 v140, v140
	v_exp_f32_e32 v141, v141
	v_exp_f32_e32 v142, v142
	v_exp_f32_e32 v143, v143
	v_pk_add_f32 v[140:141], v[140:141], 1.0 op_sel_hi:[1,0]
	v_pk_add_f32 v[142:143], v[142:143], 1.0 op_sel_hi:[1,0]
	v_rcp_f32_e32 v140, v140
	v_rcp_f32_e32 v141, v141
	v_rcp_f32_e32 v142, v142
	v_rcp_f32_e32 v143, v143
	v_lshlrev_b32_e32 v50, 16, v192
	v_and_b32_e32 v51, 0xffff0000, v192
	v_lshlrev_b32_e32 v52, 16, v193
	v_and_b32_e32 v53, 0xffff0000, v193
	v_lshlrev_b32_e32 v54, 16, v160
	v_and_b32_e32 v55, 0xffff0000, v160
	v_lshlrev_b32_e32 v56, 16, v161
	v_and_b32_e32 v57, 0xffff0000, v161
	v_pk_fma_f32 v[50:51], v[140:141], v[54:55], v[50:51]
	v_pk_fma_f32 v[52:53], v[142:143], v[56:57], v[52:53]
	v_cvt_pk_bf16_f32 v192, v50, v51
	v_cvt_pk_bf16_f32 v193, v52, v53
	v_pk_fma_f32 v[164:165], v[50:51], v[50:51], v[164:165]
	v_pk_fma_f32 v[164:165], v[52:53], v[52:53], v[164:165]
	v_pk_mul_f32 v[136:137], v[136:137], s[42:43]
	v_pk_mul_f32 v[138:139], v[138:139], s[42:43]
	v_exp_f32_e32 v136, v136
	v_exp_f32_e32 v137, v137
	v_exp_f32_e32 v138, v138
	v_exp_f32_e32 v139, v139
	v_pk_add_f32 v[136:137], v[136:137], 1.0 op_sel_hi:[1,0]
	v_pk_add_f32 v[138:139], v[138:139], 1.0 op_sel_hi:[1,0]
	v_rcp_f32_e32 v136, v136
	v_rcp_f32_e32 v137, v137
	v_rcp_f32_e32 v138, v138
	v_rcp_f32_e32 v139, v139
	v_lshlrev_b32_e32 v50, 16, v194
	v_and_b32_e32 v51, 0xffff0000, v194
	v_lshlrev_b32_e32 v52, 16, v195
	v_and_b32_e32 v53, 0xffff0000, v195
	v_lshlrev_b32_e32 v54, 16, v162
	v_and_b32_e32 v55, 0xffff0000, v162
	v_lshlrev_b32_e32 v56, 16, v163
	v_and_b32_e32 v57, 0xffff0000, v163
	v_pk_fma_f32 v[50:51], v[136:137], v[54:55], v[50:51]
	v_pk_fma_f32 v[52:53], v[138:139], v[56:57], v[52:53]
	v_cvt_pk_bf16_f32 v194, v50, v51
	v_cvt_pk_bf16_f32 v195, v52, v53
	v_pk_fma_f32 v[164:165], v[50:51], v[50:51], v[164:165]
	v_pk_fma_f32 v[164:165], v[52:53], v[52:53], v[164:165]
	v_add_f32_e32 v164, v164, v165
	global_load_dwordx4 v[172:175], v[58:59], off
	global_load_dwordx4 v[168:171], v[58:59], off offset:256
	global_load_dwordx4 v[140:143], v[60:61], off
	global_load_dwordx4 v[136:139], v[60:61], off offset:256
	v_add_co_u32_e32 v58, vcc, 0x8000, v58
	s_nop 1
	v_addc_co_u32_e32 v59, vcc, 0, v59, vcc
	v_add_co_u32_e32 v60, vcc, 0x8000, v60
	s_nop 1
	v_addc_co_u32_e32 v61, vcc, 0, v61, vcc
	global_store_dwordx4 v[62:63], v[72:75], off
	global_store_dwordx4 v[62:63], v[192:195], off offset:256
	v_add_co_u32_e32 v62, vcc, 0x28000, v62
	s_nop 1
	v_addc_co_u32_e32 v63, vcc, 0, v63, vcc
	s_waitcnt vmcnt(14)
	v_pk_mul_f32 v[132:133], v[132:133], s[42:43]
	v_pk_mul_f32 v[134:135], v[134:135], s[42:43]
	v_exp_f32_e32 v132, v132
	v_exp_f32_e32 v133, v133
	v_exp_f32_e32 v134, v134
	v_exp_f32_e32 v135, v135
	v_pk_add_f32 v[132:133], v[132:133], 1.0 op_sel_hi:[1,0]
	v_pk_add_f32 v[134:135], v[134:135], 1.0 op_sel_hi:[1,0]
	v_rcp_f32_e32 v132, v132
	v_rcp_f32_e32 v133, v133
	v_rcp_f32_e32 v134, v134
	v_rcp_f32_e32 v135, v135
	v_lshlrev_b32_e32 v50, 16, v188
	v_and_b32_e32 v51, 0xffff0000, v188
	v_lshlrev_b32_e32 v52, 16, v189
	v_and_b32_e32 v53, 0xffff0000, v189
	v_lshlrev_b32_e32 v54, 16, v156
	v_and_b32_e32 v55, 0xffff0000, v156
	v_lshlrev_b32_e32 v56, 16, v157
	v_and_b32_e32 v57, 0xffff0000, v157
	v_pk_fma_f32 v[50:51], v[132:133], v[54:55], v[50:51]
	v_pk_fma_f32 v[52:53], v[134:135], v[56:57], v[52:53]
	v_cvt_pk_bf16_f32 v188, v50, v51
	v_cvt_pk_bf16_f32 v189, v52, v53
	v_pk_mul_f32 v[156:157], v[50:51], v[50:51]
	v_pk_fma_f32 v[156:157], v[52:53], v[52:53], v[156:157]
	v_pk_mul_f32 v[128:129], v[128:129], s[42:43]
	v_pk_mul_f32 v[130:131], v[130:131], s[42:43]
	v_exp_f32_e32 v128, v128
	v_exp_f32_e32 v129, v129
	v_exp_f32_e32 v130, v130
	v_exp_f32_e32 v131, v131
	v_pk_add_f32 v[128:129], v[128:129], 1.0 op_sel_hi:[1,0]
	v_pk_add_f32 v[130:131], v[130:131], 1.0 op_sel_hi:[1,0]
	v_rcp_f32_e32 v128, v128
	v_rcp_f32_e32 v129, v129
	v_rcp_f32_e32 v130, v130
	v_rcp_f32_e32 v131, v131
	v_lshlrev_b32_e32 v50, 16, v190
	v_and_b32_e32 v51, 0xffff0000, v190
	v_lshlrev_b32_e32 v52, 16, v191
	v_and_b32_e32 v53, 0xffff0000, v191
	v_lshlrev_b32_e32 v54, 16, v158
	v_and_b32_e32 v55, 0xffff0000, v158
	v_lshlrev_b32_e32 v56, 16, v159
	v_and_b32_e32 v57, 0xffff0000, v159
	v_pk_fma_f32 v[50:51], v[128:129], v[54:55], v[50:51]
	v_pk_fma_f32 v[52:53], v[130:131], v[56:57], v[52:53]
	v_cvt_pk_bf16_f32 v190, v50, v51
	v_cvt_pk_bf16_f32 v191, v52, v53
	v_pk_fma_f32 v[156:157], v[50:51], v[50:51], v[156:157]
	v_pk_fma_f32 v[156:157], v[52:53], v[52:53], v[156:157]
	v_pk_mul_f32 v[100:101], v[100:101], s[42:43]
	v_pk_mul_f32 v[102:103], v[102:103], s[42:43]
	v_exp_f32_e32 v100, v100
	v_exp_f32_e32 v101, v101
	v_exp_f32_e32 v102, v102
	v_exp_f32_e32 v103, v103
	v_pk_add_f32 v[100:101], v[100:101], 1.0 op_sel_hi:[1,0]
	v_pk_add_f32 v[102:103], v[102:103], 1.0 op_sel_hi:[1,0]
	v_rcp_f32_e32 v100, v100
	v_rcp_f32_e32 v101, v101
	v_rcp_f32_e32 v102, v102
	v_rcp_f32_e32 v103, v103
	v_lshlrev_b32_e32 v50, 16, v184
	v_and_b32_e32 v51, 0xffff0000, v184
	v_lshlrev_b32_e32 v52, 16, v185
	v_and_b32_e32 v53, 0xffff0000, v185
	v_lshlrev_b32_e32 v54, 16, v152
	v_and_b32_e32 v55, 0xffff0000, v152
	v_lshlrev_b32_e32 v56, 16, v153
	v_and_b32_e32 v57, 0xffff0000, v153
	v_pk_fma_f32 v[50:51], v[100:101], v[54:55], v[50:51]
	v_pk_fma_f32 v[52:53], v[102:103], v[56:57], v[52:53]
	v_cvt_pk_bf16_f32 v184, v50, v51
	v_cvt_pk_bf16_f32 v185, v52, v53
	v_pk_fma_f32 v[156:157], v[50:51], v[50:51], v[156:157]
	v_pk_fma_f32 v[156:157], v[52:53], v[52:53], v[156:157]
	v_pk_mul_f32 v[96:97], v[96:97], s[42:43]
	v_pk_mul_f32 v[98:99], v[98:99], s[42:43]
	v_exp_f32_e32 v96, v96
	v_exp_f32_e32 v97, v97
	v_exp_f32_e32 v98, v98
	v_exp_f32_e32 v99, v99
	v_pk_add_f32 v[96:97], v[96:97], 1.0 op_sel_hi:[1,0]
	v_pk_add_f32 v[98:99], v[98:99], 1.0 op_sel_hi:[1,0]
	v_rcp_f32_e32 v96, v96
	v_rcp_f32_e32 v97, v97
	v_rcp_f32_e32 v98, v98
	v_rcp_f32_e32 v99, v99
	v_lshlrev_b32_e32 v50, 16, v186
	v_and_b32_e32 v51, 0xffff0000, v186
	v_lshlrev_b32_e32 v52, 16, v187
	v_and_b32_e32 v53, 0xffff0000, v187
	v_lshlrev_b32_e32 v54, 16, v154
	v_and_b32_e32 v55, 0xffff0000, v154
	v_lshlrev_b32_e32 v56, 16, v155
	v_and_b32_e32 v57, 0xffff0000, v155
	v_pk_fma_f32 v[50:51], v[96:97], v[54:55], v[50:51]
	v_pk_fma_f32 v[52:53], v[98:99], v[56:57], v[52:53]
	v_cvt_pk_bf16_f32 v186, v50, v51
	v_cvt_pk_bf16_f32 v187, v52, v53
	v_pk_fma_f32 v[156:157], v[50:51], v[50:51], v[156:157]
	v_pk_fma_f32 v[156:157], v[52:53], v[52:53], v[156:157]
	v_add_f32_e32 v156, v156, v157
	global_load_dwordx4 v[132:135], v[58:59], off
	global_load_dwordx4 v[128:131], v[58:59], off offset:256
	global_load_dwordx4 v[100:103], v[60:61], off
	global_load_dwordx4 v[96:99], v[60:61], off offset:256
	global_store_dwordx4 v[62:63], v[188:191], off
	global_store_dwordx4 v[62:63], v[184:187], off offset:256
	v_add_co_u32_e32 v62, vcc, 0x8000, v62
	s_nop 1
	v_addc_co_u32_e32 v63, vcc, 0, v63, vcc
	s_waitcnt vmcnt(14)
	v_pk_mul_f32 v[124:125], v[124:125], s[42:43]
	v_pk_mul_f32 v[126:127], v[126:127], s[42:43]
	v_exp_f32_e32 v124, v124
	v_exp_f32_e32 v125, v125
	v_exp_f32_e32 v126, v126
	v_exp_f32_e32 v127, v127
	v_pk_add_f32 v[124:125], v[124:125], 1.0 op_sel_hi:[1,0]
	v_pk_add_f32 v[126:127], v[126:127], 1.0 op_sel_hi:[1,0]
	v_rcp_f32_e32 v124, v124
	v_rcp_f32_e32 v125, v125
	v_rcp_f32_e32 v126, v126
	v_rcp_f32_e32 v127, v127
	v_lshlrev_b32_e32 v50, 16, v180
	v_and_b32_e32 v51, 0xffff0000, v180
	v_lshlrev_b32_e32 v52, 16, v181
	v_and_b32_e32 v53, 0xffff0000, v181
	v_lshlrev_b32_e32 v54, 16, v148
	v_and_b32_e32 v55, 0xffff0000, v148
	v_lshlrev_b32_e32 v56, 16, v149
	v_and_b32_e32 v57, 0xffff0000, v149
	v_pk_fma_f32 v[50:51], v[124:125], v[54:55], v[50:51]
	v_pk_fma_f32 v[52:53], v[126:127], v[56:57], v[52:53]
	v_cvt_pk_bf16_f32 v180, v50, v51
	v_cvt_pk_bf16_f32 v181, v52, v53
	v_pk_mul_f32 v[148:149], v[50:51], v[50:51]
	v_pk_fma_f32 v[148:149], v[52:53], v[52:53], v[148:149]
	v_pk_mul_f32 v[120:121], v[120:121], s[42:43]
	v_pk_mul_f32 v[122:123], v[122:123], s[42:43]
	v_exp_f32_e32 v120, v120
	v_exp_f32_e32 v121, v121
	v_exp_f32_e32 v122, v122
	v_exp_f32_e32 v123, v123
	v_pk_add_f32 v[120:121], v[120:121], 1.0 op_sel_hi:[1,0]
	v_pk_add_f32 v[122:123], v[122:123], 1.0 op_sel_hi:[1,0]
	v_rcp_f32_e32 v120, v120
	v_rcp_f32_e32 v121, v121
	v_rcp_f32_e32 v122, v122
	v_rcp_f32_e32 v123, v123
	v_lshlrev_b32_e32 v50, 16, v182
	v_and_b32_e32 v51, 0xffff0000, v182
	v_lshlrev_b32_e32 v52, 16, v183
	v_and_b32_e32 v53, 0xffff0000, v183
	v_lshlrev_b32_e32 v54, 16, v150
	v_and_b32_e32 v55, 0xffff0000, v150
	v_lshlrev_b32_e32 v56, 16, v151
	v_and_b32_e32 v57, 0xffff0000, v151
	v_pk_fma_f32 v[50:51], v[120:121], v[54:55], v[50:51]
	v_pk_fma_f32 v[52:53], v[122:123], v[56:57], v[52:53]
	v_cvt_pk_bf16_f32 v182, v50, v51
	v_cvt_pk_bf16_f32 v183, v52, v53
	v_pk_fma_f32 v[148:149], v[50:51], v[50:51], v[148:149]
	v_pk_fma_f32 v[148:149], v[52:53], v[52:53], v[148:149]
	v_pk_mul_f32 v[92:93], v[92:93], s[42:43]
	v_pk_mul_f32 v[94:95], v[94:95], s[42:43]
	v_exp_f32_e32 v92, v92
	v_exp_f32_e32 v93, v93
	v_exp_f32_e32 v94, v94
	v_exp_f32_e32 v95, v95
	v_pk_add_f32 v[92:93], v[92:93], 1.0 op_sel_hi:[1,0]
	v_pk_add_f32 v[94:95], v[94:95], 1.0 op_sel_hi:[1,0]
	v_rcp_f32_e32 v92, v92
	v_rcp_f32_e32 v93, v93
	v_rcp_f32_e32 v94, v94
	v_rcp_f32_e32 v95, v95
	v_lshlrev_b32_e32 v50, 16, v176
	v_and_b32_e32 v51, 0xffff0000, v176
	v_lshlrev_b32_e32 v52, 16, v177
	v_and_b32_e32 v53, 0xffff0000, v177
	v_lshlrev_b32_e32 v54, 16, v144
	v_and_b32_e32 v55, 0xffff0000, v144
	v_lshlrev_b32_e32 v56, 16, v145
	v_and_b32_e32 v57, 0xffff0000, v145
	v_pk_fma_f32 v[50:51], v[92:93], v[54:55], v[50:51]
	v_pk_fma_f32 v[52:53], v[94:95], v[56:57], v[52:53]
	v_cvt_pk_bf16_f32 v176, v50, v51
	v_cvt_pk_bf16_f32 v177, v52, v53
	v_pk_fma_f32 v[148:149], v[50:51], v[50:51], v[148:149]
	v_pk_fma_f32 v[148:149], v[52:53], v[52:53], v[148:149]
	v_pk_mul_f32 v[88:89], v[88:89], s[42:43]
	v_pk_mul_f32 v[90:91], v[90:91], s[42:43]
	v_exp_f32_e32 v88, v88
	v_exp_f32_e32 v89, v89
	v_exp_f32_e32 v90, v90
	v_exp_f32_e32 v91, v91
	v_pk_add_f32 v[88:89], v[88:89], 1.0 op_sel_hi:[1,0]
	v_pk_add_f32 v[90:91], v[90:91], 1.0 op_sel_hi:[1,0]
	v_rcp_f32_e32 v88, v88
	v_rcp_f32_e32 v89, v89
	v_rcp_f32_e32 v90, v90
	v_rcp_f32_e32 v91, v91
	v_lshlrev_b32_e32 v50, 16, v178
	v_and_b32_e32 v51, 0xffff0000, v178
	v_lshlrev_b32_e32 v52, 16, v179
	v_and_b32_e32 v53, 0xffff0000, v179
	v_lshlrev_b32_e32 v54, 16, v146
	v_and_b32_e32 v55, 0xffff0000, v146
	v_lshlrev_b32_e32 v56, 16, v147
	v_and_b32_e32 v57, 0xffff0000, v147
	v_pk_fma_f32 v[50:51], v[88:89], v[54:55], v[50:51]
	v_pk_fma_f32 v[52:53], v[90:91], v[56:57], v[52:53]
	v_cvt_pk_bf16_f32 v178, v50, v51
	v_cvt_pk_bf16_f32 v179, v52, v53
	v_pk_fma_f32 v[148:149], v[50:51], v[50:51], v[148:149]
	v_pk_fma_f32 v[148:149], v[52:53], v[52:53], v[148:149]
	v_add_f32_e32 v148, v148, v149
	global_store_dwordx4 v[62:63], v[180:183], off
	global_store_dwordx4 v[62:63], v[176:179], off offset:256
	v_add_co_u32_e32 v62, vcc, 0x8000, v62
	s_nop 1
	v_addc_co_u32_e32 v63, vcc, 0, v63, vcc
	s_waitcnt vmcnt(10)
	v_pk_mul_f32 v[116:117], v[116:117], s[42:43]
	v_pk_mul_f32 v[118:119], v[118:119], s[42:43]
	v_exp_f32_e32 v116, v116
	v_exp_f32_e32 v117, v117
	v_exp_f32_e32 v118, v118
	v_exp_f32_e32 v119, v119
	v_pk_add_f32 v[116:117], v[116:117], 1.0 op_sel_hi:[1,0]
	v_pk_add_f32 v[118:119], v[118:119], 1.0 op_sel_hi:[1,0]
	v_rcp_f32_e32 v116, v116
	v_rcp_f32_e32 v117, v117
	v_rcp_f32_e32 v118, v118
	v_rcp_f32_e32 v119, v119
	v_lshlrev_b32_e32 v50, 16, v172
	v_and_b32_e32 v51, 0xffff0000, v172
	v_lshlrev_b32_e32 v52, 16, v173
	v_and_b32_e32 v53, 0xffff0000, v173
	v_lshlrev_b32_e32 v54, 16, v140
	v_and_b32_e32 v55, 0xffff0000, v140
	v_lshlrev_b32_e32 v56, 16, v141
	v_and_b32_e32 v57, 0xffff0000, v141
	v_pk_fma_f32 v[50:51], v[116:117], v[54:55], v[50:51]
	v_pk_fma_f32 v[52:53], v[118:119], v[56:57], v[52:53]
	v_cvt_pk_bf16_f32 v172, v50, v51
	v_cvt_pk_bf16_f32 v173, v52, v53
	v_pk_mul_f32 v[140:141], v[50:51], v[50:51]
	v_pk_fma_f32 v[140:141], v[52:53], v[52:53], v[140:141]
	v_pk_mul_f32 v[112:113], v[112:113], s[42:43]
	v_pk_mul_f32 v[114:115], v[114:115], s[42:43]
	v_exp_f32_e32 v112, v112
	v_exp_f32_e32 v113, v113
	v_exp_f32_e32 v114, v114
	v_exp_f32_e32 v115, v115
	v_pk_add_f32 v[112:113], v[112:113], 1.0 op_sel_hi:[1,0]
	v_pk_add_f32 v[114:115], v[114:115], 1.0 op_sel_hi:[1,0]
	v_rcp_f32_e32 v112, v112
	v_rcp_f32_e32 v113, v113
	v_rcp_f32_e32 v114, v114
	v_rcp_f32_e32 v115, v115
	v_lshlrev_b32_e32 v50, 16, v174
	v_and_b32_e32 v51, 0xffff0000, v174
	v_lshlrev_b32_e32 v52, 16, v175
	v_and_b32_e32 v53, 0xffff0000, v175
	v_lshlrev_b32_e32 v54, 16, v142
	v_and_b32_e32 v55, 0xffff0000, v142
	v_lshlrev_b32_e32 v56, 16, v143
	v_and_b32_e32 v57, 0xffff0000, v143
	v_pk_fma_f32 v[50:51], v[112:113], v[54:55], v[50:51]
	v_pk_fma_f32 v[52:53], v[114:115], v[56:57], v[52:53]
	v_cvt_pk_bf16_f32 v174, v50, v51
	v_cvt_pk_bf16_f32 v175, v52, v53
	v_pk_fma_f32 v[140:141], v[50:51], v[50:51], v[140:141]
	v_pk_fma_f32 v[140:141], v[52:53], v[52:53], v[140:141]
	v_pk_mul_f32 v[84:85], v[84:85], s[42:43]
	v_pk_mul_f32 v[86:87], v[86:87], s[42:43]
	v_exp_f32_e32 v84, v84
	v_exp_f32_e32 v85, v85
	v_exp_f32_e32 v86, v86
	v_exp_f32_e32 v87, v87
	v_pk_add_f32 v[84:85], v[84:85], 1.0 op_sel_hi:[1,0]
	v_pk_add_f32 v[86:87], v[86:87], 1.0 op_sel_hi:[1,0]
	v_rcp_f32_e32 v84, v84
	v_rcp_f32_e32 v85, v85
	v_rcp_f32_e32 v86, v86
	v_rcp_f32_e32 v87, v87
	v_lshlrev_b32_e32 v50, 16, v168
	v_and_b32_e32 v51, 0xffff0000, v168
	v_lshlrev_b32_e32 v52, 16, v169
	v_and_b32_e32 v53, 0xffff0000, v169
	v_lshlrev_b32_e32 v54, 16, v136
	v_and_b32_e32 v55, 0xffff0000, v136
	v_lshlrev_b32_e32 v56, 16, v137
	v_and_b32_e32 v57, 0xffff0000, v137
	v_pk_fma_f32 v[50:51], v[84:85], v[54:55], v[50:51]
	v_pk_fma_f32 v[52:53], v[86:87], v[56:57], v[52:53]
	v_cvt_pk_bf16_f32 v168, v50, v51
	v_cvt_pk_bf16_f32 v169, v52, v53
	v_pk_fma_f32 v[140:141], v[50:51], v[50:51], v[140:141]
	v_pk_fma_f32 v[140:141], v[52:53], v[52:53], v[140:141]
	v_pk_mul_f32 v[80:81], v[80:81], s[42:43]
	v_pk_mul_f32 v[82:83], v[82:83], s[42:43]
	v_exp_f32_e32 v80, v80
	v_exp_f32_e32 v81, v81
	v_exp_f32_e32 v82, v82
	v_exp_f32_e32 v83, v83
	v_pk_add_f32 v[80:81], v[80:81], 1.0 op_sel_hi:[1,0]
	v_pk_add_f32 v[82:83], v[82:83], 1.0 op_sel_hi:[1,0]
	v_rcp_f32_e32 v80, v80
	v_rcp_f32_e32 v81, v81
	v_rcp_f32_e32 v82, v82
	v_rcp_f32_e32 v83, v83
	v_lshlrev_b32_e32 v50, 16, v170
	v_and_b32_e32 v51, 0xffff0000, v170
	v_lshlrev_b32_e32 v52, 16, v171
	v_and_b32_e32 v53, 0xffff0000, v171
	v_lshlrev_b32_e32 v54, 16, v138
	v_and_b32_e32 v55, 0xffff0000, v138
	v_lshlrev_b32_e32 v56, 16, v139
	v_and_b32_e32 v57, 0xffff0000, v139
	v_pk_fma_f32 v[50:51], v[80:81], v[54:55], v[50:51]
	v_pk_fma_f32 v[52:53], v[82:83], v[56:57], v[52:53]
	v_cvt_pk_bf16_f32 v170, v50, v51
	v_cvt_pk_bf16_f32 v171, v52, v53
	v_pk_fma_f32 v[140:141], v[50:51], v[50:51], v[140:141]
	v_pk_fma_f32 v[140:141], v[52:53], v[52:53], v[140:141]
	v_add_f32_e32 v140, v140, v141
	global_store_dwordx4 v[62:63], v[172:175], off
	global_store_dwordx4 v[62:63], v[168:171], off offset:256
	v_add_co_u32_e32 v62, vcc, 0x8000, v62
	s_nop 1
	v_addc_co_u32_e32 v63, vcc, 0, v63, vcc
	s_waitcnt vmcnt(6)
	v_pk_mul_f32 v[108:109], v[108:109], s[42:43]
	v_pk_mul_f32 v[110:111], v[110:111], s[42:43]
	v_exp_f32_e32 v108, v108
	v_exp_f32_e32 v109, v109
	v_exp_f32_e32 v110, v110
	v_exp_f32_e32 v111, v111
	v_pk_add_f32 v[108:109], v[108:109], 1.0 op_sel_hi:[1,0]
	v_pk_add_f32 v[110:111], v[110:111], 1.0 op_sel_hi:[1,0]
	v_rcp_f32_e32 v108, v108
	v_rcp_f32_e32 v109, v109
	v_rcp_f32_e32 v110, v110
	v_rcp_f32_e32 v111, v111
	v_lshlrev_b32_e32 v50, 16, v132
	v_and_b32_e32 v51, 0xffff0000, v132
	v_lshlrev_b32_e32 v52, 16, v133
	v_and_b32_e32 v53, 0xffff0000, v133
	v_lshlrev_b32_e32 v54, 16, v100
	v_and_b32_e32 v55, 0xffff0000, v100
	v_lshlrev_b32_e32 v56, 16, v101
	v_and_b32_e32 v57, 0xffff0000, v101
	v_pk_fma_f32 v[50:51], v[108:109], v[54:55], v[50:51]
	v_pk_fma_f32 v[52:53], v[110:111], v[56:57], v[52:53]
	v_cvt_pk_bf16_f32 v132, v50, v51
	v_cvt_pk_bf16_f32 v133, v52, v53
	v_pk_mul_f32 v[100:101], v[50:51], v[50:51]
	v_pk_fma_f32 v[100:101], v[52:53], v[52:53], v[100:101]
	v_pk_mul_f32 v[104:105], v[104:105], s[42:43]
	v_pk_mul_f32 v[106:107], v[106:107], s[42:43]
	v_exp_f32_e32 v104, v104
	v_exp_f32_e32 v105, v105
	v_exp_f32_e32 v106, v106
	v_exp_f32_e32 v107, v107
	v_pk_add_f32 v[104:105], v[104:105], 1.0 op_sel_hi:[1,0]
	v_pk_add_f32 v[106:107], v[106:107], 1.0 op_sel_hi:[1,0]
	v_rcp_f32_e32 v104, v104
	v_rcp_f32_e32 v105, v105
	v_rcp_f32_e32 v106, v106
	v_rcp_f32_e32 v107, v107
	v_lshlrev_b32_e32 v50, 16, v134
	v_and_b32_e32 v51, 0xffff0000, v134
	v_lshlrev_b32_e32 v52, 16, v135
	v_and_b32_e32 v53, 0xffff0000, v135
	v_lshlrev_b32_e32 v54, 16, v102
	v_and_b32_e32 v55, 0xffff0000, v102
	v_lshlrev_b32_e32 v56, 16, v103
	v_and_b32_e32 v57, 0xffff0000, v103
	v_pk_fma_f32 v[50:51], v[104:105], v[54:55], v[50:51]
	v_pk_fma_f32 v[52:53], v[106:107], v[56:57], v[52:53]
	v_cvt_pk_bf16_f32 v134, v50, v51
	v_cvt_pk_bf16_f32 v135, v52, v53
	v_pk_fma_f32 v[100:101], v[50:51], v[50:51], v[100:101]
	v_pk_fma_f32 v[100:101], v[52:53], v[52:53], v[100:101]
	v_pk_mul_f32 v[76:77], v[76:77], s[42:43]
	v_pk_mul_f32 v[78:79], v[78:79], s[42:43]
	v_exp_f32_e32 v76, v76
	v_exp_f32_e32 v77, v77
	v_exp_f32_e32 v78, v78
	v_exp_f32_e32 v79, v79
	v_pk_add_f32 v[76:77], v[76:77], 1.0 op_sel_hi:[1,0]
	v_pk_add_f32 v[78:79], v[78:79], 1.0 op_sel_hi:[1,0]
	v_rcp_f32_e32 v76, v76
	v_rcp_f32_e32 v77, v77
	v_rcp_f32_e32 v78, v78
	v_rcp_f32_e32 v79, v79
	v_lshlrev_b32_e32 v50, 16, v128
	v_and_b32_e32 v51, 0xffff0000, v128
	v_lshlrev_b32_e32 v52, 16, v129
	v_and_b32_e32 v53, 0xffff0000, v129
	v_lshlrev_b32_e32 v54, 16, v96
	v_and_b32_e32 v55, 0xffff0000, v96
	v_lshlrev_b32_e32 v56, 16, v97
	v_and_b32_e32 v57, 0xffff0000, v97
	v_pk_fma_f32 v[50:51], v[76:77], v[54:55], v[50:51]
	v_pk_fma_f32 v[52:53], v[78:79], v[56:57], v[52:53]
	v_cvt_pk_bf16_f32 v128, v50, v51
	v_cvt_pk_bf16_f32 v129, v52, v53
	v_pk_fma_f32 v[100:101], v[50:51], v[50:51], v[100:101]
	v_pk_fma_f32 v[100:101], v[52:53], v[52:53], v[100:101]
	v_pk_mul_f32 v[68:69], v[68:69], s[42:43]
	v_pk_mul_f32 v[70:71], v[70:71], s[42:43]
	v_exp_f32_e32 v68, v68
	v_exp_f32_e32 v69, v69
	v_exp_f32_e32 v70, v70
	v_exp_f32_e32 v71, v71
	v_pk_add_f32 v[68:69], v[68:69], 1.0 op_sel_hi:[1,0]
	v_pk_add_f32 v[70:71], v[70:71], 1.0 op_sel_hi:[1,0]
	v_rcp_f32_e32 v68, v68
	v_rcp_f32_e32 v69, v69
	v_rcp_f32_e32 v70, v70
	v_rcp_f32_e32 v71, v71
	v_lshlrev_b32_e32 v50, 16, v130
	v_and_b32_e32 v51, 0xffff0000, v130
	v_lshlrev_b32_e32 v52, 16, v131
	v_and_b32_e32 v53, 0xffff0000, v131
	v_lshlrev_b32_e32 v54, 16, v98
	v_and_b32_e32 v55, 0xffff0000, v98
	v_lshlrev_b32_e32 v56, 16, v99
	v_and_b32_e32 v57, 0xffff0000, v99
	v_pk_fma_f32 v[50:51], v[68:69], v[54:55], v[50:51]
	v_pk_fma_f32 v[52:53], v[70:71], v[56:57], v[52:53]
	v_cvt_pk_bf16_f32 v130, v50, v51
	v_cvt_pk_bf16_f32 v131, v52, v53
	v_pk_fma_f32 v[100:101], v[50:51], v[50:51], v[100:101]
	v_pk_fma_f32 v[100:101], v[52:53], v[52:53], v[100:101]
	v_add_f32_e32 v100, v100, v101
	global_store_dwordx4 v[62:63], v[132:135], off
	global_store_dwordx4 v[62:63], v[128:131], off offset:256
	v_xor_b32_e32 v108, 16, v238
	v_xor_b32_e32 v109, 32, v238
	v_lshlrev_b32_e32 v108, 2, v108
	v_lshlrev_b32_e32 v109, 2, v109
	ds_bpermute_b32 v50, v108, v10
	ds_bpermute_b32 v51, v108, v26
	ds_bpermute_b32 v52, v108, v42
	ds_bpermute_b32 v53, v108, v164
	ds_bpermute_b32 v54, v108, v156
	ds_bpermute_b32 v55, v108, v148
	ds_bpermute_b32 v56, v108, v140
	ds_bpermute_b32 v57, v108, v100
	s_waitcnt lgkmcnt(0)
	v_add_f32_e32 v10, v10, v50
	v_add_f32_e32 v26, v26, v51
	v_add_f32_e32 v42, v42, v52
	v_add_f32_e32 v164, v164, v53
	v_add_f32_e32 v156, v156, v54
	v_add_f32_e32 v148, v148, v55
	v_add_f32_e32 v140, v140, v56
	v_add_f32_e32 v100, v100, v57
	ds_bpermute_b32 v50, v109, v10
	ds_bpermute_b32 v51, v109, v26
	ds_bpermute_b32 v52, v109, v42
	ds_bpermute_b32 v53, v109, v164
	ds_bpermute_b32 v54, v109, v156
	ds_bpermute_b32 v55, v109, v148
	ds_bpermute_b32 v56, v109, v140
	ds_bpermute_b32 v57, v109, v100
	s_waitcnt lgkmcnt(0)
	v_add_f32_e32 v10, v10, v50
	v_add_f32_e32 v26, v26, v51
	v_add_f32_e32 v42, v42, v52
	v_add_f32_e32 v164, v164, v53
	v_add_f32_e32 v156, v156, v54
	v_add_f32_e32 v148, v148, v55
	v_add_f32_e32 v140, v140, v56
	v_add_f32_e32 v100, v100, v57
	s_mov_b64 s[6:7], exec
	s_mov_b64 exec, 0xffff
	global_store_dword v[64:65], v10, off
	global_store_dword v[64:65], v26, off offset:1024
	global_store_dword v[64:65], v42, off offset:2048
	global_store_dword v[64:65], v164, off offset:3072
	v_add_co_u32_e32 v64, vcc, 0x2000, v64
	s_nop 1
	v_addc_co_u32_e32 v65, vcc, 0, v65, vcc
	global_store_dword v[64:65], v156, off
	global_store_dword v[64:65], v148, off offset:1024
	global_store_dword v[64:65], v140, off offset:2048
	global_store_dword v[64:65], v100, off offset:3072
	s_mov_b64 exec, s[6:7]
